# attention unit prologue: QK(0) MFMA chain no longer waits (vmcnt) for the 7 younger K/V LDS-DMA requests; Q rows already landed at the first barrier
# baseline (speedup 1.0000x reference)
.LBB0_334:
	s_and_b64 vcc, exec, s[60:61]
	s_cbranch_vccz .LBB0_242
	v_readlane_b32 s10, v254, 20
	s_add_u32 s10, s10, s56
	v_readlane_b32 s11, v254, 19
	s_addc_u32 s11, s11, s57
	s_add_u32 s14, s10, s58
	s_addc_u32 s15, s11, s59
	s_lshl_b64 s[90:91], s[54:55], 1
	s_add_u32 s10, s73, s90
	v_readfirstlane_b32 s11, v235
	s_addc_u32 s44, s75, s91
	s_lshr_b32 s42, s11, 6
	s_lshl_b32 s53, s42, 5
	s_mul_i32 s54, s42, 0xc000
	s_mul_hi_u32 s55, s53, 0x600
	s_lshl_b64 vcc, s[54:55], 1
	s_add_u32 s62, s10, vcc_lo
	s_addc_u32 s63, s44, vcc_hi
	s_lshl_b32 s10, s42, 4
	v_add_u32_e32 v165, s10, v208
	v_and_or_b32 v0, s10, 48, v201
	s_lshr_b32 s10, s11, 3
	s_and_b32 s10, s10, 0x1fffffe0
	s_lshl_b32 s44, s42, 10
	v_mov_b32_e32 v2, s10
	s_movk_i32 s10, 0x180
	s_cmp_lg_u32 0, -1
	v_mad_u32_u24 v0, v0, s10, v2
	s_cselect_b32 s10, 0, 0
	s_add_i32 s70, s44, s10
	v_or_b32_e32 v0, v0, v209
	s_add_i32 s10, s70, 0xc000
	s_mov_b32 m0, s70
	s_nop 0
	global_load_lds_dwordx4 v165, s[88:89]
	v_lshlrev_b32_e32 v164, 1, v0
	s_mov_b32 m0, s10
	s_nop 0
	global_load_lds_dwordx4 v164, s[14:15]
	s_add_u32 s54, s88, 0xc000
	s_addc_u32 s55, s89, 0
	s_add_i32 s71, s70, 0x2000
	s_mov_b32 m0, s71
	s_nop 0
	global_load_lds_dwordx4 v165, s[54:55]
	global_load_dwordx4 v[140:143], v217, s[62:63]
	global_load_dwordx4 v[128:131], v217, s[62:63] offset:32
	global_load_dwordx4 v[136:139], v217, s[62:63] offset:64
	global_load_dwordx4 v[132:135], v217, s[62:63] offset:96
	s_add_u32 s64, s88, 0x18000
	s_addc_u32 s65, s89, 0
	s_add_i32 s76, s70, 0x4000
	s_waitcnt vmcnt(0) lgkmcnt(0)
	s_barrier
	s_add_u32 s62, s88, 0x24000
	s_mov_b32 m0, s76
	s_nop 0
	global_load_lds_dwordx4 v165, s[64:65]
	s_addc_u32 s63, s89, 0
	s_add_i32 s77, s70, 0x6000
	s_mov_b32 m0, s77
	s_nop 0
	global_load_lds_dwordx4 v165, s[62:63]
	s_add_u32 s62, s14, 0xc000
	s_addc_u32 s63, s15, 0
	s_add_i32 s78, s70, 0xe000
	s_mov_b32 m0, s78
	s_nop 0
	global_load_lds_dwordx4 v164, s[62:63]
	s_add_u32 s62, s88, 0x30000
	s_addc_u32 s63, s89, 0
	s_add_i32 s79, s70, 0x8000
	s_mov_b32 m0, s79
	s_nop 0
	global_load_lds_dwordx4 v165, s[62:63]
	s_add_u32 s62, s88, 0x3c000
	s_addc_u32 s63, s89, 0
	s_add_i32 s85, s70, 0xa000
	s_mov_b32 m0, s85
	s_nop 0
	global_load_lds_dwordx4 v165, s[62:63]
	s_add_u32 s62, s14, 0x18000
	s_addc_u32 s63, s15, 0
	s_add_i32 s92, s70, 0x10000
	s_mov_b32 m0, s92
	s_nop 0
	global_load_lds_dwordx4 v164, s[62:63]
	s_add_u32 s62, s14, 0x24000
	s_addc_u32 s63, s15, 0
	s_add_i32 s93, s70, 0x12000
	s_mov_b32 m0, s93
	s_nop 0
	global_load_lds_dwordx4 v164, s[62:63]
	s_waitcnt vmcnt(22)
	ds_read_b128 v[36:39], v210
	s_waitcnt vmcnt(21)
	ds_read_b128 v[40:43], v210 offset:512
	s_mov_b32 s53, s52
	s_mov_b32 s54, s52
	s_mov_b32 s55, s52
	s_mov_b32 s56, s52
	s_mov_b32 s57, s52
	s_mov_b32 s58, s52
	s_mov_b32 s59, s52
	s_mov_b32 s60, s52
	s_mov_b32 s61, s52
	s_mov_b32 s62, s52
	s_mov_b32 s63, s52
	s_mov_b32 s64, s52
	s_mov_b32 s65, s52
	s_mov_b32 s66, s52
	s_mov_b32 s67, s52
	s_waitcnt vmcnt(13)
	v_mov_b64_e32 v[4:5], s[52:53]
	v_mov_b64_e32 v[6:7], s[54:55]
	v_mov_b64_e32 v[8:9], s[56:57]
	v_mov_b64_e32 v[10:11], s[58:59]
	v_mov_b64_e32 v[12:13], s[60:61]
	v_mov_b64_e32 v[14:15], s[62:63]
	v_mov_b64_e32 v[16:17], s[64:65]
	v_mov_b64_e32 v[18:19], s[66:67]
	v_mov_b32_e32 v148, 0
	v_mov_b32_e32 v2, 0
	v_mov_b32_e32 v72, 0
	s_mov_b32 s53, -5
	s_waitcnt lgkmcnt(1)
	v_mfma_f32_32x32x16_bf16 v[20:35], v[36:39], v[140:143], v[4:19]
	s_mov_b64 s[54:55], 0
	v_mov_b32_e32 v73, 0
	v_mov_b32_e32 v149, v148
	v_mov_b32_e32 v150, v148
	v_mov_b32_e32 v151, v148
	s_waitcnt lgkmcnt(0)
	v_mfma_f32_32x32x16_bf16 v[4:19], v[40:43], v[140:143], v[4:19]
	ds_read_b128 v[36:39], v210 offset:2048
	ds_read_b128 v[40:43], v210 offset:2560
	s_waitcnt lgkmcnt(1)
	v_mfma_f32_32x32x16_bf16 v[20:35], v[36:39], v[128:131], v[20:35]
	s_waitcnt lgkmcnt(0)
	v_mfma_f32_32x32x16_bf16 v[4:19], v[40:43], v[128:131], v[4:19]
	ds_read_b128 v[36:39], v210 offset:4096
	ds_read_b128 v[40:43], v210 offset:4608
	s_waitcnt lgkmcnt(1)
	v_mfma_f32_32x32x16_bf16 v[20:35], v[36:39], v[136:139], v[20:35]
	s_waitcnt lgkmcnt(0)
	v_mfma_f32_32x32x16_bf16 v[4:19], v[40:43], v[136:139], v[4:19]
	ds_read_b128 v[36:39], v210 offset:6144
	ds_read_b128 v[40:43], v210 offset:6656
	s_waitcnt lgkmcnt(1)
	v_mfma_f32_32x32x16_bf16 v[20:35], v[36:39], v[132:135], v[20:35]
	s_waitcnt lgkmcnt(0)
	v_mfma_f32_32x32x16_bf16 v[4:19], v[40:43], v[132:135], v[4:19]
	s_nop 15
	s_nop 7
	s_waitcnt vmcnt(4) lgkmcnt(0)
	s_barrier
	ds_read_b128 v[68:71], v210 offset:8192
	ds_read_b128 v[160:163], v210 offset:8704
	ds_read_b128 v[156:159], v210 offset:10240
	ds_read_b128 v[112:115], v210 offset:10752
	ds_read_b128 v[152:155], v210 offset:12288
	ds_read_b128 v[104:107], v210 offset:12800
	ds_read_b128 v[108:111], v210 offset:14336
	ds_read_b128 v[100:103], v210 offset:14848
	s_nop 1
	v_exp_f32_e32 v52, v20
	v_exp_f32_e32 v53, v21
	v_exp_f32_e32 v54, v22
	v_exp_f32_e32 v55, v23
	v_exp_f32_e32 v56, v24
	v_exp_f32_e32 v57, v25
	v_exp_f32_e32 v58, v26
	v_exp_f32_e32 v59, v27
	v_exp_f32_e32 v60, v28
	v_exp_f32_e32 v61, v29
	v_exp_f32_e32 v62, v30
	v_exp_f32_e32 v63, v31
	v_exp_f32_e32 v64, v32
	v_exp_f32_e32 v65, v33
	v_exp_f32_e32 v66, v34
	v_exp_f32_e32 v67, v35
	v_exp_f32_e32 v36, v4
	v_exp_f32_e32 v37, v5
	v_exp_f32_e32 v38, v6
	v_exp_f32_e32 v39, v7
	v_exp_f32_e32 v40, v8
	v_exp_f32_e32 v41, v9
	v_exp_f32_e32 v42, v10
	v_exp_f32_e32 v43, v11
	v_mov_b32_e32 v44, v12
	v_mov_b32_e32 v45, v13
	v_mov_b32_e32 v46, v14
	v_mov_b32_e32 v47, v15
	v_mov_b32_e32 v48, v16
	v_mov_b32_e32 v49, v17
	v_mov_b32_e32 v50, v18
	v_mov_b32_e32 v51, v19
	s_waitcnt vmcnt(4) lgkmcnt(0)
	s_barrier
	v_mov_b32_e32 v4, 0
	v_mov_b32_e32 v5, v2
	v_mov_b32_e32 v6, v2
	v_mov_b32_e32 v7, v2
	v_mov_b32_e32 v8, v2
	v_mov_b32_e32 v9, v2
	v_mov_b32_e32 v10, v2
	v_mov_b32_e32 v11, v2
	v_mov_b32_e32 v12, v2
	v_mov_b32_e32 v13, v2
	v_mov_b32_e32 v14, v2
	v_mov_b32_e32 v15, v2
	v_mov_b32_e32 v16, v2
	v_mov_b32_e32 v17, v2
	v_mov_b32_e32 v18, v2
	v_mov_b32_e32 v19, v2
	v_mov_b32_e32 v20, 0
	v_mov_b32_e32 v21, v2
	v_mov_b32_e32 v22, v2
	v_mov_b32_e32 v23, v2
	v_mov_b32_e32 v24, v2
	v_mov_b32_e32 v25, v2
	v_mov_b32_e32 v26, v2
	v_mov_b32_e32 v27, v2
	v_mov_b32_e32 v28, v2
	v_mov_b32_e32 v29, v2
	v_mov_b32_e32 v30, v2
	v_mov_b32_e32 v31, v2
	v_mov_b32_e32 v32, v2
	v_mov_b32_e32 v33, v2
	v_mov_b32_e32 v34, v2
	v_mov_b32_e32 v35, v2
